# scan loader: each of the four value-slice units touches a distinct quarter of the next chunks Q/K cache lines ahead of the shared 16-byte loads (L2 hits for the real loads)
# baseline (speedup 1.0000x reference)
; __device__ __forceinline__ void p4_scan(const Args& a, const Frame& F) {
;     ...
;             auto conv_load = [&](int it) {
;                 const float* cW; int cN, cn;
;                 if (it < 32768) { const int e = it >> 10, sb = it & 1023; ck0 = (sb >> 6) * 64; cn = (sb & 63) * 32 + (lane & 31); cN = 2048; cW = a.in[IN_W1] + (size_t)e * 1024 * 2048; cD = (bf16*)(a.ws + WS_W1T);
;                     const int up = cn >= 1024, nn = cn & 1023; crow = e * 2048 + (nn >> 7) * 256 + up * 128 + (nn & 127); }
;                 else { const int it2 = it - 32768, e = it2 >> 9, sb = it2 & 511; ck0 = (sb >> 5) * 64; cn = (sb & 31) * 32 + (lane & 31); cN = 1024; cW = a.in[IN_W2] + (size_t)e * 1024 * 1024; cD = (bf16*)(a.ws + WS_W2T); crow = e * 1024 + cn; }
; #pragma unroll
;                 for (int i = 0; i < 32; ++i) cv[i] = cW[(size_t)(ck0 + (lane >> 5) + 2 * i) * cN + cn];
;             };
.LBB0_490:
	v_and_b32_e32 v82, 0x3c0, v9
	v_or_b32_e32 v14, v82, v158
	v_mov_b32_e32 v9, v145
	v_mul_u32_u24_e32 v12, s54, v14
	v_lshl_add_u64 v[8:9], v[8:9], 2, s[56:57]
	v_lshlrev_b32_e32 v12, 2, v12
	v_mov_b32_e32 v13, v145
	v_lshl_add_u64 v[12:13], v[8:9], 0, v[12:13]
	global_load_dword v148, v[12:13], off
	v_or_b32_e32 v12, 2, v14
	v_mul_u32_u24_e32 v12, s54, v12
	v_lshlrev_b32_e32 v12, 2, v12
	v_mov_b32_e32 v13, v145
	v_lshl_add_u64 v[12:13], v[8:9], 0, v[12:13]
	global_load_dword v141, v[12:13], off
	v_or_b32_e32 v12, 4, v14
	v_mul_u32_u24_e32 v12, s54, v12
	v_lshlrev_b32_e32 v12, 2, v12
	v_mov_b32_e32 v13, v145
	v_lshl_add_u64 v[12:13], v[8:9], 0, v[12:13]
	global_load_dword v149, v[12:13], off
	v_or_b32_e32 v12, 6, v14
	v_mul_u32_u24_e32 v12, s54, v12
	v_lshlrev_b32_e32 v12, 2, v12
	v_mov_b32_e32 v13, v145
	v_lshl_add_u64 v[12:13], v[8:9], 0, v[12:13]
	global_load_dword v137, v[12:13], off
	v_or_b32_e32 v12, 8, v14
	v_mul_u32_u24_e32 v12, s54, v12
	v_lshlrev_b32_e32 v12, 2, v12
	v_mov_b32_e32 v13, v145
	v_lshl_add_u64 v[12:13], v[8:9], 0, v[12:13]
	global_load_dword v142, v[12:13], off
	v_or_b32_e32 v12, 10, v14
	v_mul_u32_u24_e32 v12, s54, v12
	v_lshlrev_b32_e32 v12, 2, v12
	v_mov_b32_e32 v13, v145
	v_lshl_add_u64 v[12:13], v[8:9], 0, v[12:13]
	global_load_dword v81, v[12:13], off
	v_or_b32_e32 v12, 12, v14
	v_mul_u32_u24_e32 v12, s54, v12
	v_lshlrev_b32_e32 v12, 2, v12
	v_mov_b32_e32 v13, v145
	v_lshl_add_u64 v[12:13], v[8:9], 0, v[12:13]
	global_load_dword v138, v[12:13], off
	v_or_b32_e32 v12, 14, v14
	v_mul_u32_u24_e32 v12, s54, v12
	v_lshlrev_b32_e32 v12, 2, v12
	v_mov_b32_e32 v13, v145
	v_lshl_add_u64 v[12:13], v[8:9], 0, v[12:13]
	global_load_dword v151, v[12:13], off
	v_or_b32_e32 v12, 16, v14
	v_mul_u32_u24_e32 v12, s54, v12
	v_lshlrev_b32_e32 v12, 2, v12
	v_mov_b32_e32 v13, v145
	v_lshl_add_u64 v[12:13], v[8:9], 0, v[12:13]
	global_load_dword v152, v[12:13], off
	v_or_b32_e32 v12, 18, v14
	v_mul_u32_u24_e32 v12, s54, v12
	v_lshlrev_b32_e32 v12, 2, v12
	v_mov_b32_e32 v13, v145
	v_lshl_add_u64 v[12:13], v[8:9], 0, v[12:13]
	global_load_dword v143, v[12:13], off
	v_or_b32_e32 v12, 20, v14
	v_mul_u32_u24_e32 v12, s54, v12
	v_lshlrev_b32_e32 v12, 2, v12
	v_mov_b32_e32 v13, v145
	v_lshl_add_u64 v[12:13], v[8:9], 0, v[12:13]
	global_load_dword v150, v[12:13], off
	v_or_b32_e32 v12, 22, v14
	v_mul_u32_u24_e32 v12, s54, v12
	v_lshlrev_b32_e32 v12, 2, v12
	v_mov_b32_e32 v13, v145
	v_lshl_add_u64 v[12:13], v[8:9], 0, v[12:13]
	global_load_dword v139, v[12:13], off
	v_or_b32_e32 v12, 24, v14
	v_mul_u32_u24_e32 v12, s54, v12
	v_lshlrev_b32_e32 v12, 2, v12
	v_mov_b32_e32 v13, v145
	v_lshl_add_u64 v[12:13], v[8:9], 0, v[12:13]
	global_load_dword v147, v[12:13], off
	v_or_b32_e32 v12, 26, v14
	v_mul_u32_u24_e32 v12, s54, v12
	v_lshlrev_b32_e32 v12, 2, v12
	v_mov_b32_e32 v13, v145
	v_lshl_add_u64 v[12:13], v[8:9], 0, v[12:13]
	global_load_dword v83, v[12:13], off
	v_or_b32_e32 v12, 28, v14
	v_mul_u32_u24_e32 v12, s54, v12
	v_lshlrev_b32_e32 v12, 2, v12
	v_mov_b32_e32 v13, v145
	v_lshl_add_u64 v[12:13], v[8:9], 0, v[12:13]
	global_load_dword v140, v[12:13], off
	v_or_b32_e32 v12, 30, v14
	v_mul_u32_u24_e32 v12, s54, v12
	v_lshlrev_b32_e32 v12, 2, v12
	v_mov_b32_e32 v13, v145
	v_lshl_add_u64 v[12:13], v[8:9], 0, v[12:13]
	global_load_dword v153, v[12:13], off
	v_or_b32_e32 v12, 32, v14
	v_mul_u32_u24_e32 v12, s54, v12
	v_lshlrev_b32_e32 v12, 2, v12
	v_mov_b32_e32 v13, v145
	v_lshl_add_u64 v[12:13], v[8:9], 0, v[12:13]
	global_load_dword v183, v[12:13], off
	v_or_b32_e32 v12, 34, v14
	v_mul_u32_u24_e32 v12, s54, v12
	v_lshlrev_b32_e32 v12, 2, v12
	v_mov_b32_e32 v13, v145
	v_lshl_add_u64 v[12:13], v[8:9], 0, v[12:13]
	global_load_dword v179, v[12:13], off
	v_or_b32_e32 v12, 36, v14
	v_mul_u32_u24_e32 v12, s54, v12
	v_lshlrev_b32_e32 v12, 2, v12
	v_mov_b32_e32 v13, v145
	v_lshl_add_u64 v[12:13], v[8:9], 0, v[12:13]
	global_load_dword v184, v[12:13], off
	v_or_b32_e32 v12, 38, v14
	v_mul_u32_u24_e32 v12, s54, v12
	v_lshlrev_b32_e32 v12, 2, v12
	v_mov_b32_e32 v13, v145
	v_lshl_add_u64 v[12:13], v[8:9], 0, v[12:13]
	global_load_dword v175, v[12:13], off
	v_or_b32_e32 v12, 40, v14
	v_mul_u32_u24_e32 v12, s54, v12
	v_lshlrev_b32_e32 v12, 2, v12
	v_mov_b32_e32 v13, v145
	v_lshl_add_u64 v[12:13], v[8:9], 0, v[12:13]
	global_load_dword v180, v[12:13], off
	v_or_b32_e32 v12, 42, v14
	v_mul_u32_u24_e32 v12, s54, v12
	v_lshlrev_b32_e32 v12, 2, v12
	v_mov_b32_e32 v13, v145
	v_lshl_add_u64 v[12:13], v[8:9], 0, v[12:13]
	global_load_dword v173, v[12:13], off
	v_or_b32_e32 v12, 44, v14
	v_mul_u32_u24_e32 v12, s54, v12
	v_lshlrev_b32_e32 v12, 2, v12
	v_mov_b32_e32 v13, v145
	v_lshl_add_u64 v[12:13], v[8:9], 0, v[12:13]
	global_load_dword v176, v[12:13], off
	v_or_b32_e32 v12, 46, v14
	v_mul_u32_u24_e32 v12, s54, v12
	v_lshlrev_b32_e32 v12, 2, v12
	v_mov_b32_e32 v13, v145
	v_lshl_add_u64 v[12:13], v[8:9], 0, v[12:13]
	global_load_dword v186, v[12:13], off
	v_or_b32_e32 v12, 48, v14
	v_mul_u32_u24_e32 v12, s54, v12
	v_lshlrev_b32_e32 v12, 2, v12
	v_mov_b32_e32 v13, v145
	v_lshl_add_u64 v[12:13], v[8:9], 0, v[12:13]
	global_load_dword v187, v[12:13], off
	v_or_b32_e32 v12, 50, v14
	v_mul_u32_u24_e32 v12, s54, v12
	v_lshlrev_b32_e32 v12, 2, v12
	v_mov_b32_e32 v13, v145
	v_lshl_add_u64 v[12:13], v[8:9], 0, v[12:13]
	global_load_dword v181, v[12:13], off
	v_or_b32_e32 v12, 52, v14
	v_mul_u32_u24_e32 v12, s54, v12
	v_lshlrev_b32_e32 v12, 2, v12
	v_mov_b32_e32 v13, v145
	v_lshl_add_u64 v[12:13], v[8:9], 0, v[12:13]
	global_load_dword v185, v[12:13], off
	v_or_b32_e32 v12, 54, v14
	v_mul_u32_u24_e32 v12, s54, v12
	v_lshlrev_b32_e32 v12, 2, v12
	v_mov_b32_e32 v13, v145
; __device__ __forceinline__ void p4_scan(const Args& a, const Frame& F) {
;     ...
;         auto chunk_base = [&](int ci) -> int { if (ci < 2) { const int cx = dir ? (1 - ci) : ci; return T + b * CTXL + cx * 128; } const int cx = dir ? (63 - (ci - 2)) : (ci - 2); return b * SEQ + cx * 128; };
;     ...
;                 for (int i = 0; i < 8; ++i) { const int p = ht + 256 * i, row = p >> 4, c16 = p & 15; const int tok = base + (dir ? 127 - row : row);
;                     pq[i] = *(const u32x4*)(QKC + (size_t)tok * 1024 + h * 128 + c16 * 8); pk[i] = *(const u32x4*)(QKC + (size_t)tok * 1024 + 512 + h * 128 + c16 * 8); }
; #pragma unroll
;                 for (int i = 0; i < 2; ++i) { const int p = ht + 256 * i, row = p >> 2, cc = p & 3; const int tok = base + (dir ? 127 - row : row);
;                     pv[i] = *(const u32x4*)(PV + (size_t)tok * 512 + h * 128 + vs * 32 + cc * 8); pga[i] = GS[(size_t)hd * TA + tok]; }
; #pragma unroll
;                 for (int i = 0; i < 2; ++i) { const int idx = ht + 256 * i; if (idx < 384) { const int row = idx & 127, arr = idx >> 7; const int tok = base + (dir ? 127 - row : row); pgl[i] = GS[(size_t)(arr * 8 + hd) * TA + tok]; } }
;                 pbt = CH[(hd * 528 + (base >> 7)) * 2]; ppx = CH[(hd * 528 + (base >> 7)) * 2 + 1];
	v_lshl_add_u64 v[12:13], v[8:9], 0, v[12:13]
	global_load_dword v177, v[12:13], off
	v_or_b32_e32 v12, 56, v14
	v_mul_u32_u24_e32 v12, s54, v12
	v_lshlrev_b32_e32 v12, 2, v12
	v_mov_b32_e32 v13, v145
	v_lshl_add_u64 v[12:13], v[8:9], 0, v[12:13]
	global_load_dword v182, v[12:13], off
	v_or_b32_e32 v12, 58, v14
	v_mul_u32_u24_e32 v12, s54, v12
	v_lshlrev_b32_e32 v12, 2, v12
	v_mov_b32_e32 v13, v145
	v_lshl_add_u64 v[12:13], v[8:9], 0, v[12:13]
	global_load_dword v174, v[12:13], off
	v_or_b32_e32 v12, 60, v14
	v_mul_u32_u24_e32 v12, s54, v12
	v_lshlrev_b32_e32 v12, 2, v12
	v_mov_b32_e32 v13, v145
	v_lshl_add_u64 v[12:13], v[8:9], 0, v[12:13]
	global_load_dword v178, v[12:13], off
	v_or_b32_e32 v12, 62, v14
	v_mul_u32_u24_e32 v12, s54, v12
	v_lshlrev_b32_e32 v12, 2, v12
	v_mov_b32_e32 v13, v145
	v_lshl_add_u64 v[8:9], v[8:9], 0, v[12:13]
	global_load_dword v188, v[8:9], off
	s_lshl_b32 s44, s44, 1
	s_add_u32 s54, s20, s44
	s_addc_u32 s55, s21, 0
	s_lshl_b32 s33, s33, 1
	s_add_u32 s54, s54, s33
	s_addc_u32 s55, s55, 0
	v_mov_b32_e32 v87, v145
	v_lshl_add_u64 v[86:87], s[54:55], 0, v[86:87]
	s_add_i32 s54, s34, s35
	v_mov_b64_e32 v[8:9], s[38:39]
	s_add_i32 s33, 0, 0x23430
	v_mad_i64_i32 v[88:89], s[34:35], v88, s95, v[8:9]
	v_mad_i64_i32 v[90:91], s[34:35], v90, s95, v[8:9]
	s_add_i32 s54, s54, 0x10000
	v_add_u32_e32 v12, s33, v11
	s_lshl_b32 s33, s58, 13
	s_xor_b32 s34, s54, 0x80
	s_add_u32 s54, s16, s44
	v_add_u32_e32 v11, s89, v11
	s_addc_u32 s55, s17, 0
	v_lshl_add_u64 v[92:93], s[54:55], 0, v[144:145]
	s_mov_b32 s44, 0
	v_mov_b32_e32 v136, 0
	v_add_u32_e32 v134, v12, v10
	v_add_u32_e32 v135, v11, v10
	v_add_u32_e32 v214, s34, v96
	v_ashrrev_i32_e32 v215, 31, v214
	v_lshlrev_b64 v[214:215], 11, v[214:215]
	v_lshl_add_u64 v[214:215], v[92:93], 0, v[214:215]
	global_load_dwordx4 v[220:223], v[214:215], off offset:1024
	v_add_u32_e32 v214, s34, v97
	v_ashrrev_i32_e32 v215, 31, v214
	v_lshlrev_b64 v[214:215], 11, v[214:215]
	v_lshl_add_u64 v[214:215], v[92:93], 0, v[214:215]
	global_load_dwordx4 v[224:227], v[214:215], off offset:1024
	v_add_u32_e32 v214, s34, v98
	v_ashrrev_i32_e32 v215, 31, v214
	v_lshlrev_b64 v[214:215], 11, v[214:215]
	v_lshl_add_u64 v[214:215], v[92:93], 0, v[214:215]
	global_load_dwordx4 v[228:231], v[214:215], off offset:1024
	v_add_u32_e32 v214, s34, v99
	v_ashrrev_i32_e32 v215, 31, v214
	v_lshlrev_b64 v[214:215], 11, v[214:215]
	v_lshl_add_u64 v[214:215], v[92:93], 0, v[214:215]
	global_load_dwordx4 v[232:235], v[214:215], off offset:1024
	v_add_u32_e32 v214, s34, v100
	v_ashrrev_i32_e32 v215, 31, v214
	v_lshlrev_b64 v[214:215], 11, v[214:215]
	v_lshl_add_u64 v[214:215], v[92:93], 0, v[214:215]
	global_load_dwordx4 v[236:239], v[214:215], off offset:1024
	v_add_u32_e32 v214, s34, v101
	v_ashrrev_i32_e32 v215, 31, v214
	v_lshlrev_b64 v[214:215], 11, v[214:215]
	v_lshl_add_u64 v[214:215], v[92:93], 0, v[214:215]
	global_load_dwordx4 v[240:243], v[214:215], off offset:1024
	v_add_u32_e32 v214, s34, v102
	v_ashrrev_i32_e32 v215, 31, v214
	v_lshlrev_b64 v[214:215], 11, v[214:215]
	v_lshl_add_u64 v[214:215], v[92:93], 0, v[214:215]
	global_load_dwordx4 v[244:247], v[214:215], off offset:1024
	v_add_u32_e32 v214, s34, v103
	v_ashrrev_i32_e32 v215, 31, v214
	v_lshlrev_b64 v[214:215], 11, v[214:215]
	v_lshl_add_u64 v[214:215], v[92:93], 0, v[214:215]
	global_load_dwordx4 v[248:251], v[214:215], off offset:1024
	v_add_u32_e32 v214, s34, v96
	v_ashrrev_i32_e32 v215, 31, v214
	v_lshlrev_b64 v[214:215], 11, v[214:215]
	v_lshl_add_u64 v[214:215], v[92:93], 0, v[214:215]
	global_load_dwordx4 v[16:19], v[214:215], off
	v_add_u32_e32 v214, s34, v97
	v_ashrrev_i32_e32 v215, 31, v214
	v_lshlrev_b64 v[214:215], 11, v[214:215]
	v_lshl_add_u64 v[214:215], v[92:93], 0, v[214:215]
	global_load_dwordx4 v[20:23], v[214:215], off
	v_add_u32_e32 v214, s34, v98
	v_ashrrev_i32_e32 v215, 31, v214
	v_lshlrev_b64 v[214:215], 11, v[214:215]
	v_lshl_add_u64 v[214:215], v[92:93], 0, v[214:215]
	global_load_dwordx4 v[24:27], v[214:215], off
	v_add_u32_e32 v214, s34, v99
	v_ashrrev_i32_e32 v215, 31, v214
	v_lshlrev_b64 v[214:215], 11, v[214:215]
	v_lshl_add_u64 v[214:215], v[92:93], 0, v[214:215]
	global_load_dwordx4 v[28:31], v[214:215], off
	v_add_u32_e32 v214, s34, v100
	v_ashrrev_i32_e32 v215, 31, v214
	v_lshlrev_b64 v[214:215], 11, v[214:215]
	v_lshl_add_u64 v[214:215], v[92:93], 0, v[214:215]
	global_load_dwordx4 v[32:35], v[214:215], off
	v_add_u32_e32 v214, s34, v101
	v_ashrrev_i32_e32 v215, 31, v214
	v_lshlrev_b64 v[214:215], 11, v[214:215]
	v_lshl_add_u64 v[214:215], v[92:93], 0, v[214:215]
	global_load_dwordx4 v[36:39], v[214:215], off
	v_add_u32_e32 v214, s34, v102
	v_ashrrev_i32_e32 v215, 31, v214
	v_lshlrev_b64 v[214:215], 11, v[214:215]
	v_lshl_add_u64 v[214:215], v[92:93], 0, v[214:215]
	global_load_dwordx4 v[40:43], v[214:215], off
	v_add_u32_e32 v214, s34, v103
	v_ashrrev_i32_e32 v215, 31, v214
	v_lshlrev_b64 v[214:215], 11, v[214:215]
	v_lshl_add_u64 v[214:215], v[92:93], 0, v[214:215]
	global_load_dwordx4 v[44:47], v[214:215], off
	s_lshr_b32 s100, s97, 3
	s_and_b32 s100, s100, 3
	s_lshl_b32 s100, s100, 5
	v_lshrrev_b32_e32 v216, 3, v156
	v_add_u32_e32 v216, s100, v216
	v_sub_u32_e32 v217, 0x7f, v216
	v_cndmask_b32_e64 v216, v217, v216, s[4:5]
	s_lshr_b32 s100, s97, 6
	s_and_b32 s100, s100, 3
	s_lshl_b32 s100, s100, 8
	v_and_b32_e32 v217, 1, v156
	v_lshlrev_b32_e32 v217, 7, v217
	v_add_u32_e32 v212, s100, v217
	v_mov_b32_e32 v213, 0
	v_lshl_add_u64 v[212:213], s[16:17], 0, v[212:213]
	s_mov_b32 s101, 0
	s_add_i32 s101, s101, 2
	s_min_i32 s101, s101, 0x41
	s_sub_i32 s100, 0x41, s101
	s_add_i32 s101, s101, -2
	s_and_b64 vcc, s[4:5], exec
	s_cselect_b32 s101, s101, s100
	s_lshl_b32 s101, s101, 7
	s_add_i32 s101, s101, s33
	v_add_u32_e32 v214, s101, v216
	v_ashrrev_i32_e32 v215, 31, v214
	v_lshlrev_b64 v[214:215], 11, v[214:215]
	v_lshl_add_u64 v[214:215], v[212:213], 0, v[214:215]
	global_load_dword v218, v[214:215], off offset:1024
	s_branch .LBB0_492

; __device__ __forceinline__ void p4_scan(const Args& a, const Frame& F) {
;     ...
;                 for (int i = 0; i < 8; ++i) { const int p = ht + 256 * i, row = p >> 4, c16 = p & 15; const int tok = base + (dir ? 127 - row : row);
;                     pq[i] = *(const u32x4*)(QKC + (size_t)tok * 1024 + h * 128 + c16 * 8); pk[i] = *(const u32x4*)(QKC + (size_t)tok * 1024 + 512 + h * 128 + c16 * 8); }
; #pragma unroll
;                 for (int i = 0; i < 2; ++i) { const int p = ht + 256 * i, row = p >> 2, cc = p & 3; const int tok = base + (dir ? 127 - row : row);
;                     pv[i] = *(const u32x4*)(PV + (size_t)tok * 512 + h * 128 + vs * 32 + cc * 8); pga[i] = GS[(size_t)hd * TA + tok]; }
; #pragma unroll
;                 for (int i = 0; i < 2; ++i) { const int idx = ht + 256 * i; if (idx < 384) { const int row = idx & 127, arr = idx >> 7; const int tok = base + (dir ? 127 - row : row); pgl[i] = GS[(size_t)(arr * 8 + hd) * TA + tok]; } }
;                 pbt = CH[(hd * 528 + (base >> 7)) * 2]; ppx = CH[(hd * 528 + (base >> 7)) * 2 + 1];
;     ...
;             for (int ci = 0; ci < 66; ++ci) {
;                 const float M127 = fmaxf(pmx, mcar), mnew = btot + M127;
;                 const int cnx = ci + 1 < 66 ? ci + 1 : 65;
;                 prefetch(cnx);
.LBB0_492:
	s_waitcnt vmcnt(9)
	s_add_i32 s100, s44, 2
	s_min_i32 s100, s100, 0x41
	s_sub_i32 s101, 0x41, s100
	s_add_i32 s100, s100, -2
	s_and_b64 vcc, s[4:5], exec
	s_cselect_b32 s100, s100, s101
	s_lshl_b32 s100, s100, 7
	s_add_i32 s100, s100, s33
	v_add_u32_e32 v214, s100, v216
	v_ashrrev_i32_e32 v215, 31, v214
	v_lshlrev_b64 v[214:215], 11, v[214:215]
	v_lshl_add_u64 v[214:215], v[212:213], 0, v[214:215]
	global_load_dword v218, v[214:215], off
	s_add_i32 s35, s44, 1
	s_cmpk_eq_i32 s44, 0x41
	s_cselect_b32 s56, s44, s35
	s_sub_i32 s58, 0x41, s56
	v_sub_co_u32_e64 v8, s[54:55], s56, 2
	s_and_b64 s[56:57], s[4:5], exec
	v_readfirstlane_b32 s56, v8
	s_cselect_b32 s56, s56, s58
	s_lshl_b32 s56, s56, 7
	s_add_i32 s56, s56, s33
	s_and_b64 s[54:55], s[54:55], exec
	s_cselect_b32 s56, s34, s56
	v_add_u32_e32 v8, s56, v104
	v_ashrrev_i32_e32 v9, 31, v8
	v_lshlrev_b64 v[10:11], 10, v[8:9]
	v_lshl_add_u64 v[10:11], v[86:87], 0, v[10:11]
	v_lshl_add_u64 v[8:9], v[8:9], 2, s[50:51]
	global_load_dwordx4 v[12:15], v[10:11], off
	global_load_dword v172, v[8:9], off
	v_add_u32_e32 v8, s56, v105
	v_ashrrev_i32_e32 v9, 31, v8
	v_lshlrev_b64 v[10:11], 10, v[8:9]
	v_lshl_add_u64 v[10:11], v[86:87], 0, v[10:11]
	v_lshl_add_u64 v[94:95], v[8:9], 2, s[50:51]
	global_load_dwordx4 v[8:11], v[10:11], off
	s_nop 0
	global_load_dword v171, v[94:95], off
	v_or_b32_e32 v94, s56, v106
	v_ashrrev_i32_e32 v95, 31, v94
	s_and_saveexec_b64 s[54:55], s[6:7]
	s_cbranch_execz .LBB0_494
	v_lshl_add_u64 v[190:191], v[94:95], 2, v[88:89]
	global_load_dword v108, v[190:191], off

; __device__ __forceinline__ void p4_scan(const Args& a, const Frame& F) {
;     ...
;             auto conv_load = [&](int it) {
;                 const float* cW; int cN, cn;
;                 if (it < 32768) { const int e = it >> 10, sb = it & 1023; ck0 = (sb >> 6) * 64; cn = (sb & 63) * 32 + (lane & 31); cN = 2048; cW = a.in[IN_W1] + (size_t)e * 1024 * 2048; cD = (bf16*)(a.ws + WS_W1T);
;                     const int up = cn >= 1024, nn = cn & 1023; crow = e * 2048 + (nn >> 7) * 256 + up * 128 + (nn & 127); }
;                 else { const int it2 = it - 32768, e = it2 >> 9, sb = it2 & 511; ck0 = (sb >> 5) * 64; cn = (sb & 31) * 32 + (lane & 31); cN = 1024; cW = a.in[IN_W2] + (size_t)e * 1024 * 1024; cD = (bf16*)(a.ws + WS_W2T); crow = e * 1024 + cn; }
; #pragma unroll
;                 for (int i = 0; i < 32; ++i) cv[i] = cW[(size_t)(ck0 + (lane >> 5) + 2 * i) * cN + cn];
;             };
;     ...
;                 const float M127 = fmaxf(pmx, mcar), mnew = btot + M127;
;                 const int cnx = ci + 1 < 66 ? ci + 1 : 65;
;                 prefetch(cnx);
;                 commitK((ci & 1) ? S_K0 : S_K1);
;                 if (ci < 48) conv_store();
;                 conv_load(lw + 1024 * ((ci + 1) % 48));
.LBB0_502:
	s_cmp_ge_u32 s35, 48
	s_cselect_b32 s56, 0, s56
	v_and_b32_e32 v82, 0x3c0, v48
	v_max_f32_e32 v49, v136, v136
	v_max_f32_e32 v50, v85, v85
	v_or_b32_e32 v52, v82, v158
	v_max_f32_e32 v49, v50, v49
	v_mul_u32_u24_e32 v50, s56, v52
	v_add_f32_e32 v136, v84, v49
	v_lshl_add_u64 v[48:49], v[144:145], 2, s[58:59]
	v_lshlrev_b32_e32 v144, 2, v50
	v_lshl_add_u64 v[50:51], v[48:49], 0, v[144:145]
	global_load_dword v148, v[50:51], off
	v_or_b32_e32 v50, 2, v52
	v_mul_u32_u24_e32 v50, s56, v50
	v_lshlrev_b32_e32 v144, 2, v50
	v_lshl_add_u64 v[50:51], v[48:49], 0, v[144:145]
	global_load_dword v141, v[50:51], off
	v_or_b32_e32 v50, 4, v52
	v_mul_u32_u24_e32 v50, s56, v50
	v_lshlrev_b32_e32 v144, 2, v50
	v_lshl_add_u64 v[50:51], v[48:49], 0, v[144:145]
	global_load_dword v149, v[50:51], off
	v_or_b32_e32 v50, 6, v52
	v_mul_u32_u24_e32 v50, s56, v50
	v_lshlrev_b32_e32 v144, 2, v50
	v_lshl_add_u64 v[50:51], v[48:49], 0, v[144:145]
	global_load_dword v137, v[50:51], off
	v_or_b32_e32 v50, 8, v52
	v_mul_u32_u24_e32 v50, s56, v50
	v_lshlrev_b32_e32 v144, 2, v50
	v_lshl_add_u64 v[50:51], v[48:49], 0, v[144:145]
	global_load_dword v142, v[50:51], off
	v_or_b32_e32 v50, 10, v52
	v_mul_u32_u24_e32 v50, s56, v50
	v_lshlrev_b32_e32 v144, 2, v50
	v_lshl_add_u64 v[50:51], v[48:49], 0, v[144:145]
	global_load_dword v81, v[50:51], off
	v_or_b32_e32 v50, 12, v52
	v_mul_u32_u24_e32 v50, s56, v50
	v_lshlrev_b32_e32 v144, 2, v50
	v_lshl_add_u64 v[50:51], v[48:49], 0, v[144:145]
	global_load_dword v138, v[50:51], off
	v_or_b32_e32 v50, 14, v52
	v_mul_u32_u24_e32 v50, s56, v50
	v_lshlrev_b32_e32 v144, 2, v50
	v_lshl_add_u64 v[50:51], v[48:49], 0, v[144:145]
	global_load_dword v151, v[50:51], off
	v_or_b32_e32 v50, 16, v52
	v_mul_u32_u24_e32 v50, s56, v50
	v_lshlrev_b32_e32 v144, 2, v50
	v_lshl_add_u64 v[50:51], v[48:49], 0, v[144:145]
	global_load_dword v152, v[50:51], off
	v_or_b32_e32 v50, 18, v52
	v_mul_u32_u24_e32 v50, s56, v50
	v_lshlrev_b32_e32 v144, 2, v50
	v_lshl_add_u64 v[50:51], v[48:49], 0, v[144:145]
	global_load_dword v143, v[50:51], off
	v_or_b32_e32 v50, 20, v52
	v_mul_u32_u24_e32 v50, s56, v50
	v_lshlrev_b32_e32 v144, 2, v50
	v_lshl_add_u64 v[50:51], v[48:49], 0, v[144:145]
	global_load_dword v150, v[50:51], off
	v_or_b32_e32 v50, 22, v52
	v_mul_u32_u24_e32 v50, s56, v50
	v_lshlrev_b32_e32 v144, 2, v50
	v_lshl_add_u64 v[50:51], v[48:49], 0, v[144:145]
	global_load_dword v139, v[50:51], off
	v_or_b32_e32 v50, 24, v52
	v_mul_u32_u24_e32 v50, s56, v50
	v_lshlrev_b32_e32 v144, 2, v50
	v_lshl_add_u64 v[50:51], v[48:49], 0, v[144:145]
	global_load_dword v147, v[50:51], off
	v_or_b32_e32 v50, 26, v52
	v_mul_u32_u24_e32 v50, s56, v50
	v_lshlrev_b32_e32 v144, 2, v50
	v_lshl_add_u64 v[50:51], v[48:49], 0, v[144:145]
	global_load_dword v83, v[50:51], off
	v_or_b32_e32 v50, 28, v52
	v_mul_u32_u24_e32 v50, s56, v50
	v_lshlrev_b32_e32 v144, 2, v50
	v_lshl_add_u64 v[50:51], v[48:49], 0, v[144:145]
	global_load_dword v140, v[50:51], off
	v_or_b32_e32 v50, 30, v52
	v_mul_u32_u24_e32 v50, s56, v50
	v_lshlrev_b32_e32 v144, 2, v50
	v_lshl_add_u64 v[50:51], v[48:49], 0, v[144:145]
	global_load_dword v153, v[50:51], off
	v_or_b32_e32 v50, 32, v52
	v_mul_u32_u24_e32 v50, s56, v50
	v_lshlrev_b32_e32 v144, 2, v50
	v_lshl_add_u64 v[50:51], v[48:49], 0, v[144:145]
	global_load_dword v183, v[50:51], off
	v_or_b32_e32 v50, 34, v52
	v_mul_u32_u24_e32 v50, s56, v50
	v_lshlrev_b32_e32 v144, 2, v50
	v_lshl_add_u64 v[50:51], v[48:49], 0, v[144:145]
	global_load_dword v179, v[50:51], off
	v_or_b32_e32 v50, 36, v52
	v_mul_u32_u24_e32 v50, s56, v50
	v_lshlrev_b32_e32 v144, 2, v50
	v_lshl_add_u64 v[50:51], v[48:49], 0, v[144:145]
	global_load_dword v184, v[50:51], off
	v_or_b32_e32 v50, 38, v52
	v_mul_u32_u24_e32 v50, s56, v50
	v_lshlrev_b32_e32 v144, 2, v50
	v_lshl_add_u64 v[50:51], v[48:49], 0, v[144:145]
	global_load_dword v175, v[50:51], off
	v_or_b32_e32 v50, 40, v52
	v_mul_u32_u24_e32 v50, s56, v50
	v_lshlrev_b32_e32 v144, 2, v50
	v_lshl_add_u64 v[50:51], v[48:49], 0, v[144:145]
	global_load_dword v180, v[50:51], off
	v_or_b32_e32 v50, 42, v52
	v_mul_u32_u24_e32 v50, s56, v50
	v_lshlrev_b32_e32 v144, 2, v50
	v_lshl_add_u64 v[50:51], v[48:49], 0, v[144:145]
	global_load_dword v173, v[50:51], off
	v_or_b32_e32 v50, 44, v52
	v_mul_u32_u24_e32 v50, s56, v50
	v_lshlrev_b32_e32 v144, 2, v50
	v_lshl_add_u64 v[50:51], v[48:49], 0, v[144:145]
	global_load_dword v176, v[50:51], off
	v_or_b32_e32 v50, 46, v52
	v_mul_u32_u24_e32 v50, s56, v50
	v_lshlrev_b32_e32 v144, 2, v50
	v_lshl_add_u64 v[50:51], v[48:49], 0, v[144:145]
	global_load_dword v186, v[50:51], off
	v_or_b32_e32 v50, 48, v52
	v_mul_u32_u24_e32 v50, s56, v50
	v_lshlrev_b32_e32 v144, 2, v50
	v_lshl_add_u64 v[50:51], v[48:49], 0, v[144:145]
	global_load_dword v187, v[50:51], off
	v_or_b32_e32 v50, 50, v52
	v_mul_u32_u24_e32 v50, s56, v50
	v_lshlrev_b32_e32 v144, 2, v50
	v_lshl_add_u64 v[50:51], v[48:49], 0, v[144:145]
	global_load_dword v181, v[50:51], off
	v_or_b32_e32 v50, 52, v52
	v_mul_u32_u24_e32 v50, s56, v50
	v_lshlrev_b32_e32 v144, 2, v50
	v_lshl_add_u64 v[50:51], v[48:49], 0, v[144:145]
	global_load_dword v185, v[50:51], off
	v_or_b32_e32 v50, 54, v52
	v_mul_u32_u24_e32 v50, s56, v50
	v_lshlrev_b32_e32 v144, 2, v50
	v_lshl_add_u64 v[50:51], v[48:49], 0, v[144:145]
	global_load_dword v177, v[50:51], off
	v_or_b32_e32 v50, 56, v52
	v_mul_u32_u24_e32 v50, s56, v50
	v_lshlrev_b32_e32 v144, 2, v50
	v_lshl_add_u64 v[50:51], v[48:49], 0, v[144:145]
	global_load_dword v182, v[50:51], off
	v_or_b32_e32 v50, 58, v52
	v_mul_u32_u24_e32 v50, s56, v50
	v_lshlrev_b32_e32 v144, 2, v50
	v_lshl_add_u64 v[50:51], v[48:49], 0, v[144:145]
	global_load_dword v174, v[50:51], off
	v_or_b32_e32 v50, 60, v52
	v_mul_u32_u24_e32 v50, s56, v50
	v_lshlrev_b32_e32 v144, 2, v50
	v_lshl_add_u64 v[50:51], v[48:49], 0, v[144:145]
	global_load_dword v178, v[50:51], off
	v_or_b32_e32 v50, 62, v52
	v_mul_u32_u24_e32 v50, s56, v50
	v_lshlrev_b32_e32 v144, 2, v50
	v_lshl_add_u64 v[48:49], v[48:49], 0, v[144:145]
	global_load_dword v188, v[48:49], off
	s_waitcnt lgkmcnt(0)
	s_barrier
; #define LAS __attribute__((address_space(3)))
; __device__ __forceinline__ unsigned f2bf(float f) { unsigned u = __builtin_bit_cast(unsigned, f); return (u + 0x7fffu + ((u >> 16) & 1u)) >> 16; }
; __device__ __forceinline__ float bflo(unsigned w) { return __uint_as_float(w << 16); }
; __device__ __forceinline__ float bfhi(unsigned w) { return __uint_as_float(w & 0xffff0000u); }
; __device__ __forceinline__ unsigned cvt_pk_bf16(float lo, float hi) { unsigned r; asm volatile("v_cvt_pk_bf16_f32 %0, %1, %2" : "=v"(r) : "v"(lo), "v"(hi)); return r; }
; __device__ __forceinline__ void p4_scan(const Args& a, const Frame& F) {
;     ...
;             auto commitQ = [&]() {
; #pragma unroll
;                 for (int i = 0; i < 8; ++i) { const int p = ht + 256 * i, row = p >> 4, c16 = p & 15; *(LAS u32x4*)(L + S_QS + row * SP + c16 * 16) = pq[i]; } };
;             auto commitV = [&](float mprev, int vabuf) {
; #pragma unroll
;                 for (int i = 0; i < 2; ++i) { const int p = ht + 256 * i, row = p >> 2, cc = p & 3; const unsigned wv[4] = {pv[i].x, pv[i].y, pv[i].z, pv[i].w};
;                     const float av = __expf(pga[i] - fmaxf(ppx, mprev));
; #pragma unroll
;                     for (int j = 0; j < 4; ++j) { const unsigned sc2 = pg8::cvt_pk_bf16(av * bflo(wv[j]), av * bfhi(wv[j]));
;                         *(LAS bf16*)(L + S_VT + (cc * 8 + 2 * j) * SP + row * 2) = (bf16)(wv[j] & 0xffffu); *(LAS bf16*)(L + S_VT + (cc * 8 + 2 * j + 1) * SP + row * 2) = (bf16)(wv[j] >> 16);
;                         *(LAS bf16*)(L + vabuf + (cc * 8 + 2 * j) * SP + row * 2) = (bf16)(sc2 & 0xffffu); *(LAS bf16*)(L + vabuf + (cc * 8 + 2 * j + 1) * SP + row * 2) = (bf16)(sc2 >> 16); }
;                     if (cc == 0) *(LAS bf16*)(L + vabuf + 32 * SP + row * 2) = (bf16)f2bf(av); }
; #pragma unroll
;                 for (int i = 0; i < 2; ++i) { const int idx = ht + 256 * i; if (idx < 384) { const int row = idx & 127, arr = idx >> 7; *(LAS float*)(L + S_GL + arr * 512 + row * 4) = pgl[i]; } }
;             };
;     ...
;                 commitQ(); commitV(mcar, (ci & 1) ? S_VA0 : S_VA1); btot = pbt; pmx = ppx;
	s_waitcnt vmcnt(40)
	ds_write_b128 v119, v[16:19]
	ds_write_b128 v120, v[20:23]
	ds_write_b128 v121, v[24:27]
	ds_write_b128 v122, v[28:31]
	ds_write_b128 v123, v[32:35]
	ds_write_b128 v124, v[36:39]
	ds_write_b128 v125, v[40:43]
	ds_write_b128 v126, v[44:47]
	v_add_u32_e32 v214, s98, v96
	v_ashrrev_i32_e32 v215, 31, v214
	v_lshlrev_b64 v[214:215], 11, v[214:215]
	v_lshl_add_u64 v[214:215], v[92:93], 0, v[214:215]
	global_load_dwordx4 v[16:19], v[214:215], off
	v_add_u32_e32 v214, s98, v97
	v_ashrrev_i32_e32 v215, 31, v214
	v_lshlrev_b64 v[214:215], 11, v[214:215]
	v_lshl_add_u64 v[214:215], v[92:93], 0, v[214:215]
	global_load_dwordx4 v[20:23], v[214:215], off
	v_add_u32_e32 v214, s98, v98
	v_ashrrev_i32_e32 v215, 31, v214
	v_lshlrev_b64 v[214:215], 11, v[214:215]
	v_lshl_add_u64 v[214:215], v[92:93], 0, v[214:215]
	global_load_dwordx4 v[24:27], v[214:215], off
	v_add_u32_e32 v214, s98, v99
	v_ashrrev_i32_e32 v215, 31, v214
	v_lshlrev_b64 v[214:215], 11, v[214:215]
	v_lshl_add_u64 v[214:215], v[92:93], 0, v[214:215]
	global_load_dwordx4 v[28:31], v[214:215], off
	v_add_u32_e32 v214, s98, v100
	v_ashrrev_i32_e32 v215, 31, v214
	v_lshlrev_b64 v[214:215], 11, v[214:215]
	v_lshl_add_u64 v[214:215], v[92:93], 0, v[214:215]
	global_load_dwordx4 v[32:35], v[214:215], off
	v_add_u32_e32 v214, s98, v101
	v_ashrrev_i32_e32 v215, 31, v214
	v_lshlrev_b64 v[214:215], 11, v[214:215]
	v_lshl_add_u64 v[214:215], v[92:93], 0, v[214:215]
	global_load_dwordx4 v[36:39], v[214:215], off
	v_add_u32_e32 v214, s98, v102
	v_ashrrev_i32_e32 v215, 31, v214
	v_lshlrev_b64 v[214:215], 11, v[214:215]
	v_lshl_add_u64 v[214:215], v[92:93], 0, v[214:215]
	global_load_dwordx4 v[40:43], v[214:215], off
	v_add_u32_e32 v214, s98, v103
	v_ashrrev_i32_e32 v215, 31, v214
	v_lshlrev_b64 v[214:215], 11, v[214:215]
	v_lshl_add_u64 v[214:215], v[92:93], 0, v[214:215]
	global_load_dwordx4 v[44:47], v[214:215], off
	s_add_i32 s101, s35, 2
	s_min_i32 s101, s101, 0x41
	s_sub_i32 s100, 0x41, s101
	s_add_i32 s101, s101, -2
	s_and_b64 vcc, s[4:5], exec
	s_cselect_b32 s101, s101, s100
	s_lshl_b32 s101, s101, 7
	s_add_i32 s101, s101, s33
	v_add_u32_e32 v214, s101, v216
	v_ashrrev_i32_e32 v215, 31, v214
	v_lshlrev_b64 v[214:215], 11, v[214:215]
	v_lshl_add_u64 v[214:215], v[212:213], 0, v[214:215]
	global_load_dword v218, v[214:215], off offset:1024
	v_max_f32_e32 v192, v95, v95
	v_max_f32_e32 v192, v192, v136
	v_sub_f32_e32 v193, v172, v192
	v_mul_f32_e32 v193, 0x3fb8aa3b, v193
	v_exp_f32_e32 v193, v193
	s_and_b64 s[54:55], s[54:55], exec
	v_lshlrev_b32_e32 v194, 16, v12
	v_and_b32_e32 v195, 0xffff0000, v12
	s_cselect_b32 s44, 0x1de20, s92
	v_mul_f32_e32 v194, v193, v194
	v_mul_f32_e32 v195, v193, v195
	v_cvt_pk_bf16_f32 v194, v194, v195
	v_add_u32_e32 v195, v128, v129
	s_add_i32 s44, s44, 0
	ds_write_b16 v127, v12
	ds_write_b16_d16_hi v195, v12 offset:272
	v_add_u32_e32 v12, s44, v129
	v_add_u32_e32 v196, v12, v118
	ds_write_b16 v196, v194
	ds_write_b16_d16_hi v196, v194 offset:272
	v_lshlrev_b32_e32 v194, 16, v13
	v_mul_f32_e32 v194, v193, v194
	v_and_b32_e32 v197, 0xffff0000, v13
	v_mul_f32_e32 v197, v193, v197
	v_cvt_pk_bf16_f32 v194, v194, v197
	ds_write_b16 v195, v13 offset:544
	ds_write_b16_d16_hi v195, v13 offset:816
	ds_write_b16 v196, v194 offset:544
	ds_write_b16_d16_hi v196, v194 offset:816
	v_lshlrev_b32_e32 v13, 16, v14
	v_mul_f32_e32 v13, v193, v13
	v_and_b32_e32 v194, 0xffff0000, v14
	v_mul_f32_e32 v194, v193, v194
	v_cvt_pk_bf16_f32 v13, v13, v194
	ds_write_b16 v195, v14 offset:1088
	ds_write_b16_d16_hi v195, v14 offset:1360
	ds_write_b16 v196, v13 offset:1088
	ds_write_b16_d16_hi v196, v13 offset:1360
	v_lshlrev_b32_e32 v13, 16, v15
	v_mul_f32_e32 v13, v193, v13
	v_and_b32_e32 v14, 0xffff0000, v15
	v_mul_f32_e32 v14, v193, v14
	v_cvt_pk_bf16_f32 v13, v13, v14
	ds_write_b16 v195, v15 offset:1632
	ds_write_b16_d16_hi v195, v15 offset:1904
	ds_write_b16 v196, v13 offset:1632
	ds_write_b16_d16_hi v196, v13 offset:1904
	s_and_saveexec_b64 s[54:55], s[10:11]
	v_bfe_u32 v13, v193, 16, 1
	v_add3_u32 v13, v193, v13, s93
	v_add_u32_e32 v14, s44, v118
	ds_write_b16_d16_hi v14, v13 offset:8704
	s_or_b64 exec, exec, s[54:55]
	v_sub_f32_e32 v13, v171, v192
	v_mul_f32_e32 v13, 0x3fb8aa3b, v13
	v_exp_f32_e32 v13, v13
	v_lshlrev_b32_e32 v14, 16, v8
	v_and_b32_e32 v15, 0xffff0000, v8
	v_mul_f32_e32 v14, v13, v14
	v_mul_f32_e32 v15, v13, v15
	v_cvt_pk_bf16_f32 v14, v14, v15
	ds_write_b16 v131, v8
	ds_write_b16_d16_hi v132, v8 offset:272
	v_add_u32_e32 v8, v12, v130
	v_lshlrev_b32_e32 v12, 16, v9
	ds_write_b16 v8, v14
	ds_write_b16_d16_hi v8, v14 offset:272
	v_mul_f32_e32 v12, v13, v12
	v_and_b32_e32 v14, 0xffff0000, v9
	v_mul_f32_e32 v14, v13, v14
	v_cvt_pk_bf16_f32 v12, v12, v14
	ds_write_b16 v132, v9 offset:544
	ds_write_b16_d16_hi v132, v9 offset:816
	ds_write_b16 v8, v12 offset:544
	ds_write_b16_d16_hi v8, v12 offset:816
	v_lshlrev_b32_e32 v9, 16, v10
	v_mul_f32_e32 v9, v13, v9
	v_and_b32_e32 v12, 0xffff0000, v10
	v_mul_f32_e32 v12, v13, v12
	v_cvt_pk_bf16_f32 v9, v9, v12
	ds_write_b16 v132, v10 offset:1088
	ds_write_b16_d16_hi v132, v10 offset:1360
	ds_write_b16 v8, v9 offset:1088
	ds_write_b16_d16_hi v8, v9 offset:1360
	v_lshlrev_b32_e32 v9, 16, v11
	v_mul_f32_e32 v9, v13, v9
	v_and_b32_e32 v10, 0xffff0000, v11
	v_mul_f32_e32 v10, v13, v10
	v_cvt_pk_bf16_f32 v9, v9, v10
	ds_write_b16 v132, v11 offset:1632
	ds_write_b16_d16_hi v132, v11 offset:1904
	ds_write_b16 v8, v9 offset:1632
	ds_write_b16_d16_hi v8, v9 offset:1904
	s_and_saveexec_b64 s[54:55], s[10:11]
	s_cbranch_execnz .LBB0_507
	s_or_b64 exec, exec, s[54:55]
	s_and_saveexec_b64 s[54:55], s[6:7]
	s_cbranch_execnz .LBB0_508
